# prologue absorbed-weight units: the two load-wait-ds_write waterfall loops replaced by 18 back-to-back loads and a counted vmcnt ladder; on top of c6
# baseline (speedup 1.0000x reference)
.LBB0_70:
	s_ashr_i32 s12, s27, 9
	s_bfe_u32 s10, s27, 0x50004
	s_ashr_i32 s13, s12, 31
	s_waitcnt lgkmcnt(0)
	s_barrier
	s_lshl_b64 s[6:7], s[12:13], 22
	s_add_u32 s6, s2, s6
	s_addc_u32 s7, s3, s7
	s_lshl_b32 s16, s10, 17
	s_add_u32 s16, s6, s16
	s_addc_u32 s17, s7, 0
	v_ashrrev_i32_e32 v14, 5, v1
	v_lshlrev_b32_e32 v4, 2, v24
	v_and_b32_e32 v4, 0x1f0, v4
	v_lshl_add_u32 v10, v14, 9, v4
	v_lshl_add_u32 v11, v14, 14, v4
	v_mul_lo_u32 v8, v14, s23
	v_add_u32_e32 v8, v8, v4
	global_load_dwordx4 v[168:171], v10, s[16:17]
	s_add_u32 s16, s16, 0x2000
	s_addc_u32 s17, s17, 0
	global_load_dwordx4 v[172:175], v10, s[16:17]
	s_add_u32 s16, s16, 0x2000
	s_addc_u32 s17, s17, 0
	global_load_dwordx4 v[176:179], v10, s[16:17]
	s_add_u32 s16, s16, 0x2000
	s_addc_u32 s17, s17, 0
	global_load_dwordx4 v[180:183], v10, s[16:17]
	s_add_u32 s16, s16, 0x2000
	s_addc_u32 s17, s17, 0
	global_load_dwordx4 v[184:187], v10, s[16:17]
	s_add_u32 s16, s16, 0x2000
	s_addc_u32 s17, s17, 0
	global_load_dwordx4 v[188:191], v10, s[16:17]
	s_add_u32 s16, s16, 0x2000
	s_addc_u32 s17, s17, 0
	global_load_dwordx4 v[192:195], v10, s[16:17]
	s_add_u32 s16, s16, 0x2000
	s_addc_u32 s17, s17, 0
	global_load_dwordx4 v[196:199], v10, s[16:17]
	s_add_u32 s16, s16, 0x2000
	s_addc_u32 s17, s17, 0
	global_load_dwordx4 v[200:203], v10, s[16:17]
	s_add_u32 s16, s16, 0x2000
	s_addc_u32 s17, s17, 0
	global_load_dwordx4 v[204:207], v10, s[16:17]
	s_add_u32 s16, s16, 0x2000
	s_addc_u32 s17, s17, 0
	global_load_dwordx4 v[208:211], v10, s[16:17]
	s_add_u32 s16, s16, 0x2000
	s_addc_u32 s17, s17, 0
	global_load_dwordx4 v[212:215], v10, s[16:17]
	s_add_u32 s16, s16, 0x2000
	s_addc_u32 s17, s17, 0
	global_load_dwordx4 v[216:219], v10, s[16:17]
	s_add_u32 s16, s16, 0x2000
	s_addc_u32 s17, s17, 0
	global_load_dwordx4 v[16:19], v10, s[16:17]
	s_add_u32 s16, s16, 0x2000
	s_addc_u32 s17, s17, 0
	global_load_dwordx4 v[20:23], v10, s[16:17]
	s_add_u32 s16, s16, 0x2000
	s_addc_u32 s17, s17, 0
	global_load_dwordx4 v[26:29], v10, s[16:17]
	s_lshl_b32 s6, s27, 5
	s_and_b32 s29, s6, 0x1e0
	s_lshl_b64 s[16:17], s[12:13], 9
	s_or_b32 s16, s16, s29
	s_lshl_b32 s6, s10, 9
	s_add_u32 s18, s0, s6
	s_addc_u32 s19, s1, 0
	s_lshl_b64 s[16:17], s[16:17], 14
	s_add_u32 s16, s18, s16
	s_addc_u32 s17, s19, s17
	global_load_dwordx4 v[30:33], v11, s[16:17]
	s_add_u32 s16, s16, 0x40000
	s_addc_u32 s17, s17, 0
	global_load_dwordx4 v[34:37], v11, s[16:17]
	v_add_u32_e32 v9, s25, v10
	v_add_u32_e32 v12, 0x10800, v8
	s_waitcnt vmcnt(17)
	ds_write_b128 v8, v[168:171]
	s_waitcnt vmcnt(16)
	ds_write_b128 v8, v[172:175] offset:8448
	s_waitcnt vmcnt(15)
	ds_write_b128 v8, v[176:179] offset:16896
	s_waitcnt vmcnt(14)
	ds_write_b128 v8, v[180:183] offset:25344
	s_waitcnt vmcnt(13)
	ds_write_b128 v8, v[184:187] offset:33792
	s_waitcnt vmcnt(12)
	ds_write_b128 v8, v[188:191] offset:42240
	s_waitcnt vmcnt(11)
	ds_write_b128 v8, v[192:195] offset:50688
	s_waitcnt vmcnt(10)
	ds_write_b128 v8, v[196:199] offset:59136
	s_waitcnt vmcnt(9)
	ds_write_b128 v12, v[200:203]
	s_waitcnt vmcnt(8)
	ds_write_b128 v12, v[204:207] offset:8448
	s_waitcnt vmcnt(7)
	ds_write_b128 v12, v[208:211] offset:16896
	s_waitcnt vmcnt(6)
	ds_write_b128 v12, v[212:215] offset:25344
	s_waitcnt vmcnt(5)
	ds_write_b128 v12, v[216:219] offset:33792
	s_waitcnt vmcnt(4)
	ds_write_b128 v12, v[16:19] offset:42240
	s_waitcnt vmcnt(3)
	ds_write_b128 v12, v[20:23] offset:50688
	s_waitcnt vmcnt(2)
	ds_write_b128 v12, v[26:29] offset:59136
	s_waitcnt vmcnt(1)
	ds_write_b128 v9, v[30:33]
	s_waitcnt vmcnt(0)
	ds_write_b128 v9, v[34:37] offset:8192
	v_mov_b32_e32 v8, 0
	s_mov_b32 s6, 0
	v_mov_b32_e32 v9, v8
	v_mov_b32_e32 v10, v8
	v_mov_b32_e32 v11, v8
	v_mov_b32_e32 v12, v8
	v_mov_b32_e32 v13, v8
	v_mov_b32_e32 v14, v8
	v_mov_b32_e32 v15, v8
	v_mov_b32_e32 v16, v8
	v_mov_b32_e32 v17, v8
	v_mov_b32_e32 v18, v8
	v_mov_b32_e32 v19, v8
	v_mov_b32_e32 v20, v8
	v_mov_b32_e32 v21, v8
	v_mov_b32_e32 v22, v8
	v_mov_b32_e32 v23, v8
	s_waitcnt lgkmcnt(0)
	s_barrier
